# attention K/V tiles prefetched two tiles ahead; MoE counter loads issued together; scatter loop loads de-serialised; norm loops DPP
# baseline (speedup 1.0000x reference)
.LBB0_419:
	ds_bpermute_b32 v2, v226, v58
	v_max_f32_e32 v3, v58, v58
	v_max_f32_e32 v4, v57, v57
	s_mov_b64 s[8:9], 0
	v_mov_b32_e32 v248, s4
	s_waitcnt lgkmcnt(0)
	v_max_f32_e32 v2, v2, v2
	v_max_f32_e32 v2, v3, v2
	ds_bpermute_b32 v3, v226, v57
	s_mov_b32 s101, s11
	s_waitcnt lgkmcnt(0)
	s_barrier
	v_max_f32_e32 v3, v3, v3
	v_max_f32_e32 v3, v4, v3
	v_pk_add_f32 v[180:181], v[2:3], 0 neg_lo:[1,1] neg_hi:[1,1]
.LBB0_420:
	v_mov_b32_e32 v195, 0x42800000
	v_mov_b32_e32 v194, 0x358637bd
	s_and_b64 vcc, exec, s[8:9]
	s_cbranch_vccz .LBB0_422
	v_lshl_add_u32 v2, v172, 2, 0
	v_add_u32_e32 v2, 0x9000, v2
	ds_read2_b32 v[2:3], v2 offset1:32
	s_lshl_b64 s[4:5], s[18:19], 21
	s_or_b32 s8, s24, 63
	v_lshl_add_u64 v[44:45], s[4:5], 0, v[50:51]
	s_add_i32 s4, s10, 0x200
	s_or_b32 s21, s24, 31
	s_waitcnt lgkmcnt(0)
	v_pk_add_f32 v[180:181], v[2:3], v[48:49] op_sel_hi:[1,0] neg_lo:[1,1] neg_hi:[1,1]
	v_mov_b32_e32 v39, v1
	v_or3_b32 v44, v44, s52, v38
	v_mov_b32_e32 v248, s4
	s_mov_b32 s101, s8
	v_mov_b32_e32 v176, v55
	v_mov_b32_e32 v231, v47
	v_mov_b32_e32 v229, v46
	v_mov_b32_e32 v228, v43
	v_mov_b32_e32 v230, v0
.LBB0_422:
	s_lshl_b32 s52, s23, 6
	v_add_u32_e32 v2, s52, v42
	v_ashrrev_i32_e32 v3, 31, v2
	v_lshlrev_b64 v[2:3], 16, v[2:3]
	v_lshlrev_b32_e32 v0, 3, v54
	v_lshl_add_u64 v[4:5], s[14:15], 0, v[2:3]
	v_lshl_add_u64 v[4:5], s[16:17], 1, v[4:5]
	v_lshlrev_b32_e32 v0, 1, v0
	v_lshl_add_u64 v[4:5], v[4:5], 0, v[0:1]
	s_mov_b32 s4, 0x9c00000
	v_add_co_u32_e32 v4, vcc, s4, v4
	s_add_i32 s4, 0, 0x9000
	s_nop 0
	v_addc_co_u32_e32 v5, vcc, 0, v5, vcc
	global_load_dwordx4 v[144:147], v[4:5], off
	global_load_dwordx4 v[148:151], v[40:41], off
	v_add_u32_e32 v250, s4, v230
	v_lshl_add_u64 v[4:5], s[14:15], 0, v[44:45]
	s_mov_b64 s[4:5], 0x7c10000
	v_lshl_add_u64 v[216:217], v[4:5], 0, s[4:5]
	s_lshl_b64 s[4:5], s[18:19], 12
	v_lshl_add_u64 v[2:3], v[2:3], 0, s[4:5]
	v_lshl_add_u64 v[2:3], v[2:3], 0, v[38:39]
	v_lshl_add_u64 v[2:3], s[14:15], 0, v[2:3]
	s_mov_b64 s[4:5], 0x9c00080
	v_mov_b32_e32 v14, v1
	v_mov_b32_e32 v15, v1
	v_lshlrev_b32_e32 v249, 3, v49
	v_lshl_add_u64 v[218:219], v[2:3], 0, s[4:5]
	v_mov_b32_e32 v0, v1
	v_mov_b32_e32 v2, v1
	v_mov_b32_e32 v3, v1
	v_mov_b32_e32 v4, v1
	v_mov_b32_e32 v5, v1
	v_mov_b32_e32 v6, v1
	v_mov_b32_e32 v7, v1
	v_mov_b32_e32 v8, v1
	v_mov_b32_e32 v9, v1
	v_mov_b32_e32 v10, v1
	v_mov_b32_e32 v11, v1
	v_mov_b32_e32 v12, v1
	v_mov_b32_e32 v13, v1
	v_mov_b32_e32 v152, 0
	v_mov_b64_e32 v[30:31], v[14:15]
	s_waitcnt vmcnt(2)
	v_mov_b64_e32 v[46:47], v[14:15]
	v_mov_b64_e32 v[62:63], v[14:15]
	v_mov_b64_e32 v[78:79], v[14:15]
	v_lshlrev_b64 v[178:179], 9, v[174:175]
	s_mov_b32 s25, 1
	s_mov_b32 s26, 0
	v_mov_b32_e32 v182, v180
	v_mov_b32_e32 v183, v180
	v_mov_b32_e32 v184, v180
	v_mov_b32_e32 v185, v180
	v_mov_b32_e32 v186, v180
	v_mov_b32_e32 v187, v180
	v_mov_b32_e32 v188, v180
	v_mov_b32_e32 v189, v180
	v_mov_b32_e32 v190, v180
	v_mov_b32_e32 v191, v180
	v_mov_b32_e32 v192, v180
	v_mov_b32_e32 v193, v180
	v_mov_b32_e32 v198, v180
	v_mov_b32_e32 v199, v180
	v_mov_b32_e32 v200, v180
	v_mov_b32_e32 v201, v180
	v_mov_b32_e32 v180, v181
	v_mov_b32_e32 v202, v181
	v_mov_b32_e32 v203, v181
	v_mov_b32_e32 v204, v181
	v_mov_b32_e32 v205, v181
	v_mov_b32_e32 v206, v181
	v_mov_b32_e32 v207, v181
	v_mov_b32_e32 v208, v181
	v_mov_b32_e32 v209, v181
	v_mov_b32_e32 v210, v181
	v_mov_b32_e32 v211, v181
	v_mov_b32_e32 v212, v181
	v_mov_b32_e32 v213, v181
	v_mov_b32_e32 v214, v181
	v_mov_b32_e32 v215, v181
	v_mov_b32_e32 v251, 0
	v_mov_b32_e32 v238, 0
	v_mov_b64_e32 v[28:29], v[12:13]
	v_mov_b64_e32 v[26:27], v[10:11]
	v_mov_b64_e32 v[24:25], v[8:9]
	v_mov_b64_e32 v[22:23], v[6:7]
	v_mov_b64_e32 v[20:21], v[4:5]
	v_mov_b64_e32 v[18:19], v[2:3]
	v_mov_b64_e32 v[16:17], v[0:1]
	v_mov_b64_e32 v[44:45], v[12:13]
	v_mov_b64_e32 v[42:43], v[10:11]
	v_mov_b64_e32 v[40:41], v[8:9]
	v_mov_b64_e32 v[38:39], v[6:7]
	v_mov_b64_e32 v[36:37], v[4:5]
	v_mov_b64_e32 v[34:35], v[2:3]
	v_mov_b64_e32 v[32:33], v[0:1]
	v_mov_b64_e32 v[60:61], v[12:13]
	v_mov_b64_e32 v[58:59], v[10:11]
	v_mov_b64_e32 v[56:57], v[8:9]
	v_mov_b64_e32 v[54:55], v[6:7]
	v_mov_b64_e32 v[52:53], v[4:5]
	v_mov_b64_e32 v[50:51], v[2:3]
	v_mov_b64_e32 v[48:49], v[0:1]
	v_mov_b64_e32 v[76:77], v[12:13]
	v_mov_b64_e32 v[74:75], v[10:11]
	v_mov_b64_e32 v[72:73], v[8:9]
	v_mov_b64_e32 v[70:71], v[6:7]
	v_mov_b64_e32 v[68:69], v[4:5]
	v_mov_b64_e32 v[66:67], v[2:3]
	v_mov_b64_e32 v[64:65], v[0:1]
	v_mov_b32_e32 v153, v152
	v_mov_b32_e32 v154, v152
	v_mov_b32_e32 v155, v152
	v_mov_b32_e32 v2, v152
	v_mov_b32_e32 v3, v152
	v_mov_b32_e32 v4, v152
	v_mov_b32_e32 v5, v152
	v_mov_b32_e32 v6, v152
	v_mov_b32_e32 v7, v152
	v_mov_b32_e32 v8, v152
	v_mov_b32_e32 v9, v152
	v_mov_b32_e32 v10, v152
	v_mov_b32_e32 v11, v152
	v_mov_b32_e32 v12, v152
	v_mov_b32_e32 v13, v152
	global_load_dwordx4 v[240:243], v[216:217], off
	global_load_dwordx4 v[244:247], v[218:219], off
	s_branch .LBB0_426

.LBB0_426:
	s_bitcmp1_b32 s25, 0
	s_cselect_b32 s4, 0, 0x2400
	s_add_i32 s4, s4, 0
	v_add3_u32 v0, s4, v228, v229
	s_add_i32 s5, s25, 1
	s_bitcmp1_b32 s25, 0
	s_cbranch_scc0 .Lat_odd
	s_cmp_ge_u32 s25, s20
	s_cbranch_scc1 .Lat_e_w0
	s_waitcnt vmcnt(2)
	s_branch .Lat_e_w

.Lat_e_w:
	ds_write_b128 v0, v[148:151]
	ds_write_b128 v0, v[144:147] offset:18432
	s_waitcnt lgkmcnt(0)
	s_barrier
	s_cmp_ge_u32 s5, s20
	s_cbranch_scc1 .LBB0_428
	v_lshl_add_u64 v[232:233], v[216:217], 0, s[86:87]
	global_load_dwordx4 v[148:151], v[232:233], off
	global_load_dwordx4 v[144:147], v[218:219], off offset:128
	s_branch .LBB0_428
.Lat_odd:
	s_cmp_ge_u32 s25, s20
	s_cbranch_scc1 .Lat_o_w0
	s_waitcnt vmcnt(2)
	s_branch .Lat_o_w

.Lat_o_w:
	ds_write_b128 v0, v[240:243]
	ds_write_b128 v0, v[244:247] offset:18432
	s_waitcnt lgkmcnt(0)
	s_barrier
	s_cmp_ge_u32 s5, s20
	s_cbranch_scc1 .LBB0_428
	v_lshl_add_u64 v[232:233], v[216:217], 0, s[86:87]
	global_load_dwordx4 v[240:243], v[232:233], off
	global_load_dwordx4 v[244:247], v[218:219], off offset:128
.LBB0_428:
	s_cmp_gt_i32 s26, s101
	s_cbranch_scc1 .LBB0_425
	s_cmp_le_i32 s26, s21
	s_cselect_b64 s[8:9], -1, 0
	s_cmp_gt_i32 s26, s21
	s_cbranch_scc1 .LBB0_433
	v_add3_u32 v0, s4, v231, v230
	ds_read_b128 v[96:99], v250
	ds_read_b128 v[100:103], v250 offset:32
	ds_read_b128 v[104:107], v250 offset:64
	ds_read_b128 v[108:111], v250 offset:96
	ds_read_b128 v[80:83], v250 offset:128
	ds_read_b128 v[84:87], v250 offset:160
	ds_read_b128 v[88:91], v250 offset:192
	ds_read_b128 v[92:95], v250 offset:224
	ds_read_b128 v[2:5], v0
	ds_read_b128 v[6:9], v0 offset:32
	ds_read_b128 v[10:13], v0 offset:4608
	ds_read_b128 v[112:115], v0 offset:4640
	ds_read_b128 v[116:119], v0 offset:64
	ds_read_b128 v[120:123], v0 offset:96
	ds_read_b128 v[124:127], v0 offset:4672
	ds_read_b128 v[128:131], v0 offset:4704
	ds_read_b128 v[132:135], v177 offset:49152
	ds_read_b128 v[136:139], v177 offset:50176
	ds_read_b128 v[140:143], v177 offset:51200
	ds_read_b128 v[152:155], v177 offset:52224
	s_waitcnt lgkmcnt(3)
	v_mfma_f32_32x32x16_bf16 v[96:111], v[2:5], v[132:135], v[96:111]
	s_add_i32 s5, s26, 63
	s_cmp_le_i32 s5, s24
	v_mfma_f32_32x32x16_bf16 v[80:95], v[10:13], v[132:135], v[80:95]
	s_waitcnt lgkmcnt(2)
	v_mfma_f32_32x32x16_bf16 v[96:111], v[6:9], v[136:139], v[96:111]
	v_mfma_f32_32x32x16_bf16 v[80:95], v[112:115], v[136:139], v[80:95]
	s_waitcnt lgkmcnt(1)
	v_mfma_f32_32x32x16_bf16 v[96:111], v[116:119], v[140:143], v[96:111]
	v_mfma_f32_32x32x16_bf16 v[80:95], v[124:127], v[140:143], v[80:95]
	s_waitcnt lgkmcnt(0)
	v_mfma_f32_32x32x16_bf16 v[96:111], v[120:123], v[152:155], v[96:111]
	v_mfma_f32_32x32x16_bf16 v[80:95], v[128:131], v[152:155], v[80:95]
	s_cbranch_scc1 .LBB0_432
	v_add_u32_e32 v0, s26, v176
	v_add_u32_e32 v2, 32, v0
	v_cmp_le_i32_e32 vcc, v2, v172
	v_add_u32_e32 v2, 33, v0
	s_nop 6
	v_cndmask_b32_e32 v80, v239, v80, vcc
	v_cmp_lt_i32_e32 vcc, v0, v172
	s_nop 1
	v_cndmask_b32_e32 v97, v239, v97, vcc
	v_cmp_le_i32_e32 vcc, v0, v172
	s_nop 1
	v_cndmask_b32_e32 v96, v239, v96, vcc
	v_cmp_le_i32_e32 vcc, v2, v172
	v_add_u32_e32 v2, 2, v0
	s_nop 0
	v_cndmask_b32_e32 v81, v239, v81, vcc
	v_cmp_le_i32_e32 vcc, v2, v172
	v_add_u32_e32 v2, 34, v0
	s_nop 0
	v_cndmask_b32_e32 v98, v239, v98, vcc
	v_cmp_le_i32_e32 vcc, v2, v172
	v_add_u32_e32 v2, 3, v0
	s_nop 0
	v_cndmask_b32_e32 v82, v239, v82, vcc
	v_cmp_le_i32_e32 vcc, v2, v172
	v_add_u32_e32 v2, 35, v0
	s_nop 0
	v_cndmask_b32_e32 v99, v239, v99, vcc
	v_cmp_le_i32_e32 vcc, v2, v172
	v_add_u32_e32 v2, 8, v0
	s_nop 0
	v_cndmask_b32_e32 v83, v239, v83, vcc
	v_cmp_le_i32_e32 vcc, v2, v172
	v_add_u32_e32 v2, 40, v0
	s_nop 0
	v_cndmask_b32_e32 v100, v239, v100, vcc
	v_cmp_le_i32_e32 vcc, v2, v172
	v_add_u32_e32 v2, 9, v0
	s_nop 0
	v_cndmask_b32_e32 v84, v239, v84, vcc
	v_cmp_le_i32_e32 vcc, v2, v172
	v_add_u32_e32 v2, 41, v0
	s_nop 0
	v_cndmask_b32_e32 v101, v239, v101, vcc
	v_cmp_le_i32_e32 vcc, v2, v172
	v_add_u32_e32 v2, 10, v0
	s_nop 0
	v_cndmask_b32_e32 v85, v239, v85, vcc
	v_cmp_le_i32_e32 vcc, v2, v172
	v_add_u32_e32 v2, 42, v0
	s_nop 0
	v_cndmask_b32_e32 v102, v239, v102, vcc
	v_cmp_le_i32_e32 vcc, v2, v172
	v_add_u32_e32 v2, 11, v0
	s_nop 0
	v_cndmask_b32_e32 v86, v239, v86, vcc
	v_cmp_le_i32_e32 vcc, v2, v172
	v_add_u32_e32 v2, 43, v0
	s_nop 0
	v_cndmask_b32_e32 v103, v239, v103, vcc
	v_cmp_le_i32_e32 vcc, v2, v172
	v_add_u32_e32 v2, 16, v0
	s_nop 0
	v_cndmask_b32_e32 v87, v239, v87, vcc
	v_cmp_le_i32_e32 vcc, v2, v172
	v_add_u32_e32 v2, 48, v0
	s_nop 0
	v_cndmask_b32_e32 v104, v239, v104, vcc
	v_cmp_le_i32_e32 vcc, v2, v172
	v_add_u32_e32 v2, 17, v0
	s_nop 0
	v_cndmask_b32_e32 v88, v239, v88, vcc
	v_cmp_le_i32_e32 vcc, v2, v172
	v_add_u32_e32 v2, 49, v0
	s_nop 0
	v_cndmask_b32_e32 v105, v239, v105, vcc
	v_cmp_le_i32_e32 vcc, v2, v172
	v_add_u32_e32 v2, 18, v0
	s_nop 0
	v_cndmask_b32_e32 v89, v239, v89, vcc
	v_cmp_le_i32_e32 vcc, v2, v172
	v_add_u32_e32 v2, 50, v0
	s_nop 0
	v_cndmask_b32_e32 v106, v239, v106, vcc
	v_cmp_le_i32_e32 vcc, v2, v172
	v_add_u32_e32 v2, 19, v0
	s_nop 0
	v_cndmask_b32_e32 v90, v239, v90, vcc
	v_cmp_le_i32_e32 vcc, v2, v172
	v_add_u32_e32 v2, 51, v0
	s_nop 0
	v_cndmask_b32_e32 v107, v239, v107, vcc
	v_cmp_le_i32_e32 vcc, v2, v172
	v_add_u32_e32 v2, 24, v0
	s_nop 0
	v_cndmask_b32_e32 v91, v239, v91, vcc
	v_cmp_le_i32_e32 vcc, v2, v172
	v_add_u32_e32 v2, 56, v0
	s_nop 0
	v_cndmask_b32_e32 v108, v239, v108, vcc
	v_cmp_le_i32_e32 vcc, v2, v172
	v_add_u32_e32 v2, 25, v0
	s_nop 0
	v_cndmask_b32_e32 v92, v239, v92, vcc
	v_cmp_le_i32_e32 vcc, v2, v172
	v_add_u32_e32 v2, 57, v0
	s_nop 0
	v_cndmask_b32_e32 v109, v239, v109, vcc
	v_cmp_le_i32_e32 vcc, v2, v172
	v_add_u32_e32 v2, 26, v0
	s_nop 0
	v_cndmask_b32_e32 v93, v239, v93, vcc
	v_cmp_le_i32_e32 vcc, v2, v172
	v_add_u32_e32 v2, 58, v0
	s_nop 0
	v_cndmask_b32_e32 v110, v239, v110, vcc
	v_cmp_le_i32_e32 vcc, v2, v172
	v_add_u32_e32 v2, 27, v0
	v_add_u32_e32 v0, 59, v0
	v_cndmask_b32_e32 v94, v239, v94, vcc
	v_cmp_le_i32_e32 vcc, v2, v172
	s_nop 1
	v_cndmask_b32_e32 v111, v239, v111, vcc
	v_cmp_le_i32_e32 vcc, v0, v172
	s_nop 1
	v_cndmask_b32_e32 v95, v239, v95, vcc

	.amdhsa_kernel _Z10fwd_kernel4Args
		.amdhsa_group_segment_fixed_size 0
		.amdhsa_private_segment_fixed_size 0
		.amdhsa_kernarg_size 480
		.amdhsa_user_sgpr_count 2
		.amdhsa_user_sgpr_dispatch_ptr 0
		.amdhsa_user_sgpr_queue_ptr 0
		.amdhsa_user_sgpr_kernarg_segment_ptr 1
		.amdhsa_user_sgpr_dispatch_id 0
		.amdhsa_user_sgpr_kernarg_preload_length 0
		.amdhsa_user_sgpr_kernarg_preload_offset 0
		.amdhsa_user_sgpr_private_segment_size 0
		.amdhsa_uses_dynamic_stack 0
		.amdhsa_enable_private_segment 0
		.amdhsa_system_sgpr_workgroup_id_x 1
		.amdhsa_system_sgpr_workgroup_id_y 0
		.amdhsa_system_sgpr_workgroup_id_z 0
		.amdhsa_system_sgpr_workgroup_info 0
		.amdhsa_system_vgpr_workitem_id 0
		.amdhsa_next_free_vgpr 256
		.amdhsa_next_free_sgpr 102
		.amdhsa_accum_offset 256
		.amdhsa_reserve_vcc 1
		.amdhsa_float_round_mode_32 0
		.amdhsa_float_round_mode_16_64 0
		.amdhsa_float_denorm_mode_32 3
		.amdhsa_float_denorm_mode_16_64 3
		.amdhsa_dx10_clamp 1
		.amdhsa_ieee_mode 1
		.amdhsa_fp16_overflow 0
		.amdhsa_tg_split 0
		.amdhsa_exception_fp_ieee_invalid_op 0
		.amdhsa_exception_fp_denorm_src 0
		.amdhsa_exception_fp_ieee_div_zero 0
		.amdhsa_exception_fp_ieee_overflow 0
		.amdhsa_exception_fp_ieee_underflow 0
		.amdhsa_exception_fp_ieee_inexact 0
		.amdhsa_exception_int_div_zero 0
	.end_amdhsa_kernel

amdhsa.kernels:
  - .agpr_count:     0
    .args:
      - .offset:         0
        .size:           224
        .value_kind:     by_value
      - .offset:         224
        .size:           4
        .value_kind:     hidden_block_count_x
      - .offset:         228
        .size:           4
        .value_kind:     hidden_block_count_y
      - .offset:         232
        .size:           4
        .value_kind:     hidden_block_count_z
      - .offset:         236
        .size:           2
        .value_kind:     hidden_group_size_x
      - .offset:         238
        .size:           2
        .value_kind:     hidden_group_size_y
      - .offset:         240
        .size:           2
        .value_kind:     hidden_group_size_z
      - .offset:         242
        .size:           2
        .value_kind:     hidden_remainder_x
      - .offset:         244
        .size:           2
        .value_kind:     hidden_remainder_y
      - .offset:         246
        .size:           2
        .value_kind:     hidden_remainder_z
      - .offset:         264
        .size:           8
        .value_kind:     hidden_global_offset_x
      - .offset:         272
        .size:           8
        .value_kind:     hidden_global_offset_y
      - .offset:         280
        .size:           8
        .value_kind:     hidden_global_offset_z
      - .offset:         288
        .size:           2
        .value_kind:     hidden_grid_dims
      - .offset:         344
        .size:           4
        .value_kind:     hidden_dynamic_lds_size
    .group_segment_fixed_size: 0
    .kernarg_segment_align: 8
    .kernarg_segment_size: 480
    .language:       OpenCL C
    .language_version:
      - 2
      - 0
    .max_flat_workgroup_size: 512
    .name:           _Z10fwd_kernel4Args
    .private_segment_fixed_size: 0
    .sgpr_count:     108
    .sgpr_spill_count: 231
    .symbol:         _Z10fwd_kernel4Args.kd
    .uniform_work_group_size: 1
    .uses_dynamic_stack: false
    .vgpr_count:     256
    .vgpr_spill_count: 0
    .wavefront_size: 64
